# speedup vs baseline: 1.0245x; 1.0027x over previous
.LBB2_114:
	s_setprio 0
	v_and_b32_e32 v0, 16, v0
	v_lshlrev_b32_e32 v1, 2, v191
	s_lshl_b32 s0, s34, 5
	v_add_u32_e32 v70, 12, v1
	v_cmp_eq_u32_e32 vcc, 0, v0
	s_add_i32 s0, s0, s33
	s_mov_b32 s1, 0x3f3504f3
	v_cndmask_b32_e32 v0, v70, v1, vcc
	v_or_b32_e32 v0, s0, v0
	v_ashrrev_i32_e32 v1, 31, v0
	v_lshl_add_u64 v[78:79], v[0:1], 1, s[4:5]
	s_waitcnt vmcnt(0) lgkmcnt(0)
	s_mov_b32 s76, 0x3e6d3388
	s_mov_b32 s78, 0xbf38aa3b
	s_mov_b32 s80, 0x3f87dc22
	s_mov_b32 s82, 0x3fb5f0e3
	s_mov_b32 s84, 0xbe91a98e
	s_mov_b32 s86, 0x3e827906
	v_mov_b32_e32 v248, 0xbfba00e3
	v_mov_b32_e32 v249, 0xbfba00e3
	v_cmp_lt_i32_e32 vcc, -1, v218
	s_cbranch_vccz .Lepskip_0
	v_mul_f32_e32 v232, 0.5, v220
	v_pk_mul_f32 v[234:235], v[74:75], v[74:75]
	v_pk_mul_f32 v[252:253], v[76:77], v[76:77]
	v_fma_f32 v236, |v74|, s76, 1.0
	v_fma_f32 v254, |v76|, s76, 1.0
	v_fma_f32 v237, |v75|, s76, 1.0
	v_fma_f32 v255, |v77|, s76, 1.0
	v_pk_mul_f32 v[234:235], v[234:235], s[78:79] op_sel_hi:[1,0]
	v_pk_mul_f32 v[252:253], v[252:253], s[78:79] op_sel_hi:[1,0]
	v_rcp_f32_e32 v236, v236
	v_rcp_f32_e32 v254, v254
	v_rcp_f32_e32 v237, v237
	v_rcp_f32_e32 v255, v255
	v_exp_f32_e32 v234, v234
	v_exp_f32_e32 v252, v252
	v_exp_f32_e32 v235, v235
	v_exp_f32_e32 v253, v253
	v_pk_fma_f32 v[238:239], v[236:237], s[80:81], v[248:249] op_sel_hi:[1,0,1]
	v_pk_fma_f32 v[70:71], v[254:255], s[80:81], v[248:249] op_sel_hi:[1,0,1]
	v_pk_mul_f32 v[240:241], v[232:233], v[74:75] op_sel_hi:[0,1]
	v_pk_mul_f32 v[72:73], v[232:233], v[76:77] op_sel_hi:[0,1]
	v_pk_fma_f32 v[238:239], v[238:239], v[236:237], s[82:83] op_sel_hi:[1,1,0]
	v_pk_fma_f32 v[70:71], v[70:71], v[254:255], s[82:83] op_sel_hi:[1,1,0]
	v_pk_fma_f32 v[238:239], v[238:239], v[236:237], s[84:85] op_sel_hi:[1,1,0]
	v_pk_fma_f32 v[70:71], v[70:71], v[254:255], s[84:85] op_sel_hi:[1,1,0]
	v_pk_fma_f32 v[238:239], v[238:239], v[236:237], s[86:87] op_sel_hi:[1,1,0]
	v_pk_fma_f32 v[70:71], v[70:71], v[254:255], s[86:87] op_sel_hi:[1,1,0]
	v_pk_mul_f32 v[238:239], v[238:239], v[236:237]
	v_pk_mul_f32 v[70:71], v[70:71], v[254:255]
	v_pk_fma_f32 v[238:239], v[238:239], v[234:235], 1.0 op_sel_hi:[1,1,0] neg_lo:[1,0,0] neg_hi:[1,0,0]
	v_pk_fma_f32 v[70:71], v[70:71], v[252:253], 1.0 op_sel_hi:[1,1,0] neg_lo:[1,0,0] neg_hi:[1,0,0]
	v_fma_f32 v242, |v240|, v238, v240
	v_fma_f32 v0, |v72|, v70, v72
	v_fma_f32 v243, |v241|, v239, v241
	v_fma_f32 v1, |v73|, v71, v73
	v_cvt_pk_f16_f32 v244, v242, v243
	v_cvt_pk_f16_f32 v245, v0, v1
	v_pk_mul_f32 v[234:235], v[66:67], v[66:67]
	v_pk_mul_f32 v[252:253], v[68:69], v[68:69]
	v_fma_f32 v236, |v66|, s76, 1.0
	v_fma_f32 v254, |v68|, s76, 1.0
	v_fma_f32 v237, |v67|, s76, 1.0
	v_fma_f32 v255, |v69|, s76, 1.0
	v_pk_mul_f32 v[234:235], v[234:235], s[78:79] op_sel_hi:[1,0]
	v_pk_mul_f32 v[252:253], v[252:253], s[78:79] op_sel_hi:[1,0]
	v_rcp_f32_e32 v236, v236
	v_rcp_f32_e32 v254, v254
	v_rcp_f32_e32 v237, v237
	v_rcp_f32_e32 v255, v255
	v_exp_f32_e32 v234, v234
	v_exp_f32_e32 v252, v252
	v_exp_f32_e32 v235, v235
	v_exp_f32_e32 v253, v253
	v_pk_fma_f32 v[238:239], v[236:237], s[80:81], v[248:249] op_sel_hi:[1,0,1]
	v_pk_fma_f32 v[70:71], v[254:255], s[80:81], v[248:249] op_sel_hi:[1,0,1]
	v_pk_mul_f32 v[240:241], v[232:233], v[66:67] op_sel_hi:[0,1]
	v_pk_mul_f32 v[72:73], v[232:233], v[68:69] op_sel_hi:[0,1]
	v_pk_fma_f32 v[238:239], v[238:239], v[236:237], s[82:83] op_sel_hi:[1,1,0]
	v_pk_fma_f32 v[70:71], v[70:71], v[254:255], s[82:83] op_sel_hi:[1,1,0]
	v_pk_fma_f32 v[238:239], v[238:239], v[236:237], s[84:85] op_sel_hi:[1,1,0]
	v_pk_fma_f32 v[70:71], v[70:71], v[254:255], s[84:85] op_sel_hi:[1,1,0]
	v_pk_fma_f32 v[238:239], v[238:239], v[236:237], s[86:87] op_sel_hi:[1,1,0]
	v_pk_fma_f32 v[70:71], v[70:71], v[254:255], s[86:87] op_sel_hi:[1,1,0]
	v_pk_mul_f32 v[238:239], v[238:239], v[236:237]
	v_pk_mul_f32 v[70:71], v[70:71], v[254:255]
	v_pk_fma_f32 v[238:239], v[238:239], v[234:235], 1.0 op_sel_hi:[1,1,0] neg_lo:[1,0,0] neg_hi:[1,0,0]
	v_pk_fma_f32 v[70:71], v[70:71], v[252:253], 1.0 op_sel_hi:[1,1,0] neg_lo:[1,0,0] neg_hi:[1,0,0]
	v_fma_f32 v242, |v240|, v238, v240
	v_fma_f32 v0, |v72|, v70, v72
	v_fma_f32 v243, |v241|, v239, v241
	v_fma_f32 v1, |v73|, v71, v73
	v_cvt_pk_f16_f32 v246, v242, v243
	v_cvt_pk_f16_f32 v247, v0, v1
	v_cmp_lt_i32_e32 vcc, -1, v218
	s_nop 0
	v_permlane16_swap_b32_e32 v244, v246
	v_permlane16_swap_b32_e32 v245, v247
	s_and_saveexec_b64 s[10:11], vcc
	s_cbranch_execz .Lep_0
	v_mov_b32_e32 v250, v218
	v_mov_b32_e32 v251, 0
	v_lshlrev_b64 v[250:251], 10, v[250:251]
	v_lshl_add_u64 v[250:251], v[78:79], 0, v[250:251]
	global_store_dwordx4 v[250:251], v[244:247], off sc1

.Lepskip_0:
	v_cmp_lt_i32_e32 vcc, -1, v214
	s_cbranch_vccz .Lepskip_1
	v_mul_f32_e32 v232, 0.5, v216
	v_pk_mul_f32 v[234:235], v[62:63], v[62:63]
	v_pk_mul_f32 v[252:253], v[64:65], v[64:65]
	v_fma_f32 v236, |v62|, s76, 1.0
	v_fma_f32 v254, |v64|, s76, 1.0
	v_fma_f32 v237, |v63|, s76, 1.0
	v_fma_f32 v255, |v65|, s76, 1.0
	v_pk_mul_f32 v[234:235], v[234:235], s[78:79] op_sel_hi:[1,0]
	v_pk_mul_f32 v[252:253], v[252:253], s[78:79] op_sel_hi:[1,0]
	v_rcp_f32_e32 v236, v236
	v_rcp_f32_e32 v254, v254
	v_rcp_f32_e32 v237, v237
	v_rcp_f32_e32 v255, v255
	v_exp_f32_e32 v234, v234
	v_exp_f32_e32 v252, v252
	v_exp_f32_e32 v235, v235
	v_exp_f32_e32 v253, v253
	v_pk_fma_f32 v[238:239], v[236:237], s[80:81], v[248:249] op_sel_hi:[1,0,1]
	v_pk_fma_f32 v[70:71], v[254:255], s[80:81], v[248:249] op_sel_hi:[1,0,1]
	v_pk_mul_f32 v[240:241], v[232:233], v[62:63] op_sel_hi:[0,1]
	v_pk_mul_f32 v[72:73], v[232:233], v[64:65] op_sel_hi:[0,1]
	v_pk_fma_f32 v[238:239], v[238:239], v[236:237], s[82:83] op_sel_hi:[1,1,0]
	v_pk_fma_f32 v[70:71], v[70:71], v[254:255], s[82:83] op_sel_hi:[1,1,0]
	v_pk_fma_f32 v[238:239], v[238:239], v[236:237], s[84:85] op_sel_hi:[1,1,0]
	v_pk_fma_f32 v[70:71], v[70:71], v[254:255], s[84:85] op_sel_hi:[1,1,0]
	v_pk_fma_f32 v[238:239], v[238:239], v[236:237], s[86:87] op_sel_hi:[1,1,0]
	v_pk_fma_f32 v[70:71], v[70:71], v[254:255], s[86:87] op_sel_hi:[1,1,0]
	v_pk_mul_f32 v[238:239], v[238:239], v[236:237]
	v_pk_mul_f32 v[70:71], v[70:71], v[254:255]
	v_pk_fma_f32 v[238:239], v[238:239], v[234:235], 1.0 op_sel_hi:[1,1,0] neg_lo:[1,0,0] neg_hi:[1,0,0]
	v_pk_fma_f32 v[70:71], v[70:71], v[252:253], 1.0 op_sel_hi:[1,1,0] neg_lo:[1,0,0] neg_hi:[1,0,0]
	v_fma_f32 v242, |v240|, v238, v240
	v_fma_f32 v0, |v72|, v70, v72
	v_fma_f32 v243, |v241|, v239, v241
	v_fma_f32 v1, |v73|, v71, v73
	v_cvt_pk_f16_f32 v244, v242, v243
	v_cvt_pk_f16_f32 v245, v0, v1
	v_pk_mul_f32 v[234:235], v[58:59], v[58:59]
	v_pk_mul_f32 v[252:253], v[60:61], v[60:61]
	v_fma_f32 v236, |v58|, s76, 1.0
	v_fma_f32 v254, |v60|, s76, 1.0
	v_fma_f32 v237, |v59|, s76, 1.0
	v_fma_f32 v255, |v61|, s76, 1.0
	v_pk_mul_f32 v[234:235], v[234:235], s[78:79] op_sel_hi:[1,0]
	v_pk_mul_f32 v[252:253], v[252:253], s[78:79] op_sel_hi:[1,0]
	v_rcp_f32_e32 v236, v236
	v_rcp_f32_e32 v254, v254
	v_rcp_f32_e32 v237, v237
	v_rcp_f32_e32 v255, v255
	v_exp_f32_e32 v234, v234
	v_exp_f32_e32 v252, v252
	v_exp_f32_e32 v235, v235
	v_exp_f32_e32 v253, v253
	v_pk_fma_f32 v[238:239], v[236:237], s[80:81], v[248:249] op_sel_hi:[1,0,1]
	v_pk_fma_f32 v[70:71], v[254:255], s[80:81], v[248:249] op_sel_hi:[1,0,1]
	v_pk_mul_f32 v[240:241], v[232:233], v[58:59] op_sel_hi:[0,1]
	v_pk_mul_f32 v[72:73], v[232:233], v[60:61] op_sel_hi:[0,1]
	v_pk_fma_f32 v[238:239], v[238:239], v[236:237], s[82:83] op_sel_hi:[1,1,0]
	v_pk_fma_f32 v[70:71], v[70:71], v[254:255], s[82:83] op_sel_hi:[1,1,0]
	v_pk_fma_f32 v[238:239], v[238:239], v[236:237], s[84:85] op_sel_hi:[1,1,0]
	v_pk_fma_f32 v[70:71], v[70:71], v[254:255], s[84:85] op_sel_hi:[1,1,0]
	v_pk_fma_f32 v[238:239], v[238:239], v[236:237], s[86:87] op_sel_hi:[1,1,0]
	v_pk_fma_f32 v[70:71], v[70:71], v[254:255], s[86:87] op_sel_hi:[1,1,0]
	v_pk_mul_f32 v[238:239], v[238:239], v[236:237]
	v_pk_mul_f32 v[70:71], v[70:71], v[254:255]
	v_pk_fma_f32 v[238:239], v[238:239], v[234:235], 1.0 op_sel_hi:[1,1,0] neg_lo:[1,0,0] neg_hi:[1,0,0]
	v_pk_fma_f32 v[70:71], v[70:71], v[252:253], 1.0 op_sel_hi:[1,1,0] neg_lo:[1,0,0] neg_hi:[1,0,0]
	v_fma_f32 v242, |v240|, v238, v240
	v_fma_f32 v0, |v72|, v70, v72
	v_fma_f32 v243, |v241|, v239, v241
	v_fma_f32 v1, |v73|, v71, v73
	v_cvt_pk_f16_f32 v246, v242, v243
	v_cvt_pk_f16_f32 v247, v0, v1
	v_cmp_lt_i32_e32 vcc, -1, v214
	s_nop 0
	v_permlane16_swap_b32_e32 v244, v246
	v_permlane16_swap_b32_e32 v245, v247
	s_and_saveexec_b64 s[10:11], vcc
	s_cbranch_execz .Lep_1
	v_mov_b32_e32 v250, v214
	v_mov_b32_e32 v251, 0
	v_lshlrev_b64 v[250:251], 10, v[250:251]
	v_lshl_add_u64 v[250:251], v[78:79], 0, v[250:251]
	global_store_dwordx4 v[250:251], v[244:247], off sc1

.Lepskip_1:
	v_cmp_lt_i32_e32 vcc, -1, v210
	s_cbranch_vccz .Lepskip_2
	v_mul_f32_e32 v232, 0.5, v212
	v_pk_mul_f32 v[234:235], v[54:55], v[54:55]
	v_pk_mul_f32 v[252:253], v[56:57], v[56:57]
	v_fma_f32 v236, |v54|, s76, 1.0
	v_fma_f32 v254, |v56|, s76, 1.0
	v_fma_f32 v237, |v55|, s76, 1.0
	v_fma_f32 v255, |v57|, s76, 1.0
	v_pk_mul_f32 v[234:235], v[234:235], s[78:79] op_sel_hi:[1,0]
	v_pk_mul_f32 v[252:253], v[252:253], s[78:79] op_sel_hi:[1,0]
	v_rcp_f32_e32 v236, v236
	v_rcp_f32_e32 v254, v254
	v_rcp_f32_e32 v237, v237
	v_rcp_f32_e32 v255, v255
	v_exp_f32_e32 v234, v234
	v_exp_f32_e32 v252, v252
	v_exp_f32_e32 v235, v235
	v_exp_f32_e32 v253, v253
	v_pk_fma_f32 v[238:239], v[236:237], s[80:81], v[248:249] op_sel_hi:[1,0,1]
	v_pk_fma_f32 v[70:71], v[254:255], s[80:81], v[248:249] op_sel_hi:[1,0,1]
	v_pk_mul_f32 v[240:241], v[232:233], v[54:55] op_sel_hi:[0,1]
	v_pk_mul_f32 v[72:73], v[232:233], v[56:57] op_sel_hi:[0,1]
	v_pk_fma_f32 v[238:239], v[238:239], v[236:237], s[82:83] op_sel_hi:[1,1,0]
	v_pk_fma_f32 v[70:71], v[70:71], v[254:255], s[82:83] op_sel_hi:[1,1,0]
	v_pk_fma_f32 v[238:239], v[238:239], v[236:237], s[84:85] op_sel_hi:[1,1,0]
	v_pk_fma_f32 v[70:71], v[70:71], v[254:255], s[84:85] op_sel_hi:[1,1,0]
	v_pk_fma_f32 v[238:239], v[238:239], v[236:237], s[86:87] op_sel_hi:[1,1,0]
	v_pk_fma_f32 v[70:71], v[70:71], v[254:255], s[86:87] op_sel_hi:[1,1,0]
	v_pk_mul_f32 v[238:239], v[238:239], v[236:237]
	v_pk_mul_f32 v[70:71], v[70:71], v[254:255]
	v_pk_fma_f32 v[238:239], v[238:239], v[234:235], 1.0 op_sel_hi:[1,1,0] neg_lo:[1,0,0] neg_hi:[1,0,0]
	v_pk_fma_f32 v[70:71], v[70:71], v[252:253], 1.0 op_sel_hi:[1,1,0] neg_lo:[1,0,0] neg_hi:[1,0,0]
	v_fma_f32 v242, |v240|, v238, v240
	v_fma_f32 v0, |v72|, v70, v72
	v_fma_f32 v243, |v241|, v239, v241
	v_fma_f32 v1, |v73|, v71, v73
	v_cvt_pk_f16_f32 v244, v242, v243
	v_cvt_pk_f16_f32 v245, v0, v1
	v_pk_mul_f32 v[234:235], v[50:51], v[50:51]
	v_pk_mul_f32 v[252:253], v[52:53], v[52:53]
	v_fma_f32 v236, |v50|, s76, 1.0
	v_fma_f32 v254, |v52|, s76, 1.0
	v_fma_f32 v237, |v51|, s76, 1.0
	v_fma_f32 v255, |v53|, s76, 1.0
	v_pk_mul_f32 v[234:235], v[234:235], s[78:79] op_sel_hi:[1,0]
	v_pk_mul_f32 v[252:253], v[252:253], s[78:79] op_sel_hi:[1,0]
	v_rcp_f32_e32 v236, v236
	v_rcp_f32_e32 v254, v254
	v_rcp_f32_e32 v237, v237
	v_rcp_f32_e32 v255, v255
	v_exp_f32_e32 v234, v234
	v_exp_f32_e32 v252, v252
	v_exp_f32_e32 v235, v235
	v_exp_f32_e32 v253, v253
	v_pk_fma_f32 v[238:239], v[236:237], s[80:81], v[248:249] op_sel_hi:[1,0,1]
	v_pk_fma_f32 v[70:71], v[254:255], s[80:81], v[248:249] op_sel_hi:[1,0,1]
	v_pk_mul_f32 v[240:241], v[232:233], v[50:51] op_sel_hi:[0,1]
	v_pk_mul_f32 v[72:73], v[232:233], v[52:53] op_sel_hi:[0,1]
	v_pk_fma_f32 v[238:239], v[238:239], v[236:237], s[82:83] op_sel_hi:[1,1,0]
	v_pk_fma_f32 v[70:71], v[70:71], v[254:255], s[82:83] op_sel_hi:[1,1,0]
	v_pk_fma_f32 v[238:239], v[238:239], v[236:237], s[84:85] op_sel_hi:[1,1,0]
	v_pk_fma_f32 v[70:71], v[70:71], v[254:255], s[84:85] op_sel_hi:[1,1,0]
	v_pk_fma_f32 v[238:239], v[238:239], v[236:237], s[86:87] op_sel_hi:[1,1,0]
	v_pk_fma_f32 v[70:71], v[70:71], v[254:255], s[86:87] op_sel_hi:[1,1,0]
	v_pk_mul_f32 v[238:239], v[238:239], v[236:237]
	v_pk_mul_f32 v[70:71], v[70:71], v[254:255]
	v_pk_fma_f32 v[238:239], v[238:239], v[234:235], 1.0 op_sel_hi:[1,1,0] neg_lo:[1,0,0] neg_hi:[1,0,0]
	v_pk_fma_f32 v[70:71], v[70:71], v[252:253], 1.0 op_sel_hi:[1,1,0] neg_lo:[1,0,0] neg_hi:[1,0,0]
	v_fma_f32 v242, |v240|, v238, v240
	v_fma_f32 v0, |v72|, v70, v72
	v_fma_f32 v243, |v241|, v239, v241
	v_fma_f32 v1, |v73|, v71, v73
	v_cvt_pk_f16_f32 v246, v242, v243
	v_cvt_pk_f16_f32 v247, v0, v1
	v_cmp_lt_i32_e32 vcc, -1, v210
	s_nop 0
	v_permlane16_swap_b32_e32 v244, v246
	v_permlane16_swap_b32_e32 v245, v247
	s_and_saveexec_b64 s[10:11], vcc
	s_cbranch_execz .Lep_2
	v_mov_b32_e32 v250, v210
	v_mov_b32_e32 v251, 0
	v_lshlrev_b64 v[250:251], 10, v[250:251]
	v_lshl_add_u64 v[250:251], v[78:79], 0, v[250:251]
	global_store_dwordx4 v[250:251], v[244:247], off sc1

.Lepskip_2:
	v_cmp_lt_i32_e32 vcc, -1, v206
	s_cbranch_vccz .Lepskip_3
	v_mul_f32_e32 v232, 0.5, v208
	v_pk_mul_f32 v[234:235], v[46:47], v[46:47]
	v_pk_mul_f32 v[252:253], v[48:49], v[48:49]
	v_fma_f32 v236, |v46|, s76, 1.0
	v_fma_f32 v254, |v48|, s76, 1.0
	v_fma_f32 v237, |v47|, s76, 1.0
	v_fma_f32 v255, |v49|, s76, 1.0
	v_pk_mul_f32 v[234:235], v[234:235], s[78:79] op_sel_hi:[1,0]
	v_pk_mul_f32 v[252:253], v[252:253], s[78:79] op_sel_hi:[1,0]
	v_rcp_f32_e32 v236, v236
	v_rcp_f32_e32 v254, v254
	v_rcp_f32_e32 v237, v237
	v_rcp_f32_e32 v255, v255
	v_exp_f32_e32 v234, v234
	v_exp_f32_e32 v252, v252
	v_exp_f32_e32 v235, v235
	v_exp_f32_e32 v253, v253
	v_pk_fma_f32 v[238:239], v[236:237], s[80:81], v[248:249] op_sel_hi:[1,0,1]
	v_pk_fma_f32 v[70:71], v[254:255], s[80:81], v[248:249] op_sel_hi:[1,0,1]
	v_pk_mul_f32 v[240:241], v[232:233], v[46:47] op_sel_hi:[0,1]
	v_pk_mul_f32 v[72:73], v[232:233], v[48:49] op_sel_hi:[0,1]
	v_pk_fma_f32 v[238:239], v[238:239], v[236:237], s[82:83] op_sel_hi:[1,1,0]
	v_pk_fma_f32 v[70:71], v[70:71], v[254:255], s[82:83] op_sel_hi:[1,1,0]
	v_pk_fma_f32 v[238:239], v[238:239], v[236:237], s[84:85] op_sel_hi:[1,1,0]
	v_pk_fma_f32 v[70:71], v[70:71], v[254:255], s[84:85] op_sel_hi:[1,1,0]
	v_pk_fma_f32 v[238:239], v[238:239], v[236:237], s[86:87] op_sel_hi:[1,1,0]
	v_pk_fma_f32 v[70:71], v[70:71], v[254:255], s[86:87] op_sel_hi:[1,1,0]
	v_pk_mul_f32 v[238:239], v[238:239], v[236:237]
	v_pk_mul_f32 v[70:71], v[70:71], v[254:255]
	v_pk_fma_f32 v[238:239], v[238:239], v[234:235], 1.0 op_sel_hi:[1,1,0] neg_lo:[1,0,0] neg_hi:[1,0,0]
	v_pk_fma_f32 v[70:71], v[70:71], v[252:253], 1.0 op_sel_hi:[1,1,0] neg_lo:[1,0,0] neg_hi:[1,0,0]
	v_fma_f32 v242, |v240|, v238, v240
	v_fma_f32 v0, |v72|, v70, v72
	v_fma_f32 v243, |v241|, v239, v241
	v_fma_f32 v1, |v73|, v71, v73
	v_cvt_pk_f16_f32 v244, v242, v243
	v_cvt_pk_f16_f32 v245, v0, v1
	v_pk_mul_f32 v[234:235], v[42:43], v[42:43]
	v_pk_mul_f32 v[252:253], v[44:45], v[44:45]
	v_fma_f32 v236, |v42|, s76, 1.0
	v_fma_f32 v254, |v44|, s76, 1.0
	v_fma_f32 v237, |v43|, s76, 1.0
	v_fma_f32 v255, |v45|, s76, 1.0
	v_pk_mul_f32 v[234:235], v[234:235], s[78:79] op_sel_hi:[1,0]
	v_pk_mul_f32 v[252:253], v[252:253], s[78:79] op_sel_hi:[1,0]
	v_rcp_f32_e32 v236, v236
	v_rcp_f32_e32 v254, v254
	v_rcp_f32_e32 v237, v237
	v_rcp_f32_e32 v255, v255
	v_exp_f32_e32 v234, v234
	v_exp_f32_e32 v252, v252
	v_exp_f32_e32 v235, v235
	v_exp_f32_e32 v253, v253
	v_pk_fma_f32 v[238:239], v[236:237], s[80:81], v[248:249] op_sel_hi:[1,0,1]
	v_pk_fma_f32 v[70:71], v[254:255], s[80:81], v[248:249] op_sel_hi:[1,0,1]
	v_pk_mul_f32 v[240:241], v[232:233], v[42:43] op_sel_hi:[0,1]
	v_pk_mul_f32 v[72:73], v[232:233], v[44:45] op_sel_hi:[0,1]
	v_pk_fma_f32 v[238:239], v[238:239], v[236:237], s[82:83] op_sel_hi:[1,1,0]
	v_pk_fma_f32 v[70:71], v[70:71], v[254:255], s[82:83] op_sel_hi:[1,1,0]
	v_pk_fma_f32 v[238:239], v[238:239], v[236:237], s[84:85] op_sel_hi:[1,1,0]
	v_pk_fma_f32 v[70:71], v[70:71], v[254:255], s[84:85] op_sel_hi:[1,1,0]
	v_pk_fma_f32 v[238:239], v[238:239], v[236:237], s[86:87] op_sel_hi:[1,1,0]
	v_pk_fma_f32 v[70:71], v[70:71], v[254:255], s[86:87] op_sel_hi:[1,1,0]
	v_pk_mul_f32 v[238:239], v[238:239], v[236:237]
	v_pk_mul_f32 v[70:71], v[70:71], v[254:255]
	v_pk_fma_f32 v[238:239], v[238:239], v[234:235], 1.0 op_sel_hi:[1,1,0] neg_lo:[1,0,0] neg_hi:[1,0,0]
	v_pk_fma_f32 v[70:71], v[70:71], v[252:253], 1.0 op_sel_hi:[1,1,0] neg_lo:[1,0,0] neg_hi:[1,0,0]
	v_fma_f32 v242, |v240|, v238, v240
	v_fma_f32 v0, |v72|, v70, v72
	v_fma_f32 v243, |v241|, v239, v241
	v_fma_f32 v1, |v73|, v71, v73
	v_cvt_pk_f16_f32 v246, v242, v243
	v_cvt_pk_f16_f32 v247, v0, v1
	v_cmp_lt_i32_e32 vcc, -1, v206
	s_nop 0
	v_permlane16_swap_b32_e32 v244, v246
	v_permlane16_swap_b32_e32 v245, v247
	s_and_saveexec_b64 s[10:11], vcc
	s_cbranch_execz .Lep_3
	v_mov_b32_e32 v250, v206
	v_mov_b32_e32 v251, 0
	v_lshlrev_b64 v[250:251], 10, v[250:251]
	v_lshl_add_u64 v[250:251], v[78:79], 0, v[250:251]
	global_store_dwordx4 v[250:251], v[244:247], off sc1

.Lepskip_3:
	v_cmp_lt_i32_e32 vcc, -1, v202
	s_cbranch_vccz .Lepskip_4
	v_mul_f32_e32 v232, 0.5, v204
	v_pk_mul_f32 v[234:235], v[38:39], v[38:39]
	v_pk_mul_f32 v[252:253], v[40:41], v[40:41]
	v_fma_f32 v236, |v38|, s76, 1.0
	v_fma_f32 v254, |v40|, s76, 1.0
	v_fma_f32 v237, |v39|, s76, 1.0
	v_fma_f32 v255, |v41|, s76, 1.0
	v_pk_mul_f32 v[234:235], v[234:235], s[78:79] op_sel_hi:[1,0]
	v_pk_mul_f32 v[252:253], v[252:253], s[78:79] op_sel_hi:[1,0]
	v_rcp_f32_e32 v236, v236
	v_rcp_f32_e32 v254, v254
	v_rcp_f32_e32 v237, v237
	v_rcp_f32_e32 v255, v255
	v_exp_f32_e32 v234, v234
	v_exp_f32_e32 v252, v252
	v_exp_f32_e32 v235, v235
	v_exp_f32_e32 v253, v253
	v_pk_fma_f32 v[238:239], v[236:237], s[80:81], v[248:249] op_sel_hi:[1,0,1]
	v_pk_fma_f32 v[70:71], v[254:255], s[80:81], v[248:249] op_sel_hi:[1,0,1]
	v_pk_mul_f32 v[240:241], v[232:233], v[38:39] op_sel_hi:[0,1]
	v_pk_mul_f32 v[72:73], v[232:233], v[40:41] op_sel_hi:[0,1]
	v_pk_fma_f32 v[238:239], v[238:239], v[236:237], s[82:83] op_sel_hi:[1,1,0]
	v_pk_fma_f32 v[70:71], v[70:71], v[254:255], s[82:83] op_sel_hi:[1,1,0]
	v_pk_fma_f32 v[238:239], v[238:239], v[236:237], s[84:85] op_sel_hi:[1,1,0]
	v_pk_fma_f32 v[70:71], v[70:71], v[254:255], s[84:85] op_sel_hi:[1,1,0]
	v_pk_fma_f32 v[238:239], v[238:239], v[236:237], s[86:87] op_sel_hi:[1,1,0]
	v_pk_fma_f32 v[70:71], v[70:71], v[254:255], s[86:87] op_sel_hi:[1,1,0]
	v_pk_mul_f32 v[238:239], v[238:239], v[236:237]
	v_pk_mul_f32 v[70:71], v[70:71], v[254:255]
	v_pk_fma_f32 v[238:239], v[238:239], v[234:235], 1.0 op_sel_hi:[1,1,0] neg_lo:[1,0,0] neg_hi:[1,0,0]
	v_pk_fma_f32 v[70:71], v[70:71], v[252:253], 1.0 op_sel_hi:[1,1,0] neg_lo:[1,0,0] neg_hi:[1,0,0]
	v_fma_f32 v242, |v240|, v238, v240
	v_fma_f32 v0, |v72|, v70, v72
	v_fma_f32 v243, |v241|, v239, v241
	v_fma_f32 v1, |v73|, v71, v73
	v_cvt_pk_f16_f32 v244, v242, v243
	v_cvt_pk_f16_f32 v245, v0, v1
	v_pk_mul_f32 v[234:235], v[34:35], v[34:35]
	v_pk_mul_f32 v[252:253], v[36:37], v[36:37]
	v_fma_f32 v236, |v34|, s76, 1.0
	v_fma_f32 v254, |v36|, s76, 1.0
	v_fma_f32 v237, |v35|, s76, 1.0
	v_fma_f32 v255, |v37|, s76, 1.0
	v_pk_mul_f32 v[234:235], v[234:235], s[78:79] op_sel_hi:[1,0]
	v_pk_mul_f32 v[252:253], v[252:253], s[78:79] op_sel_hi:[1,0]
	v_rcp_f32_e32 v236, v236
	v_rcp_f32_e32 v254, v254
	v_rcp_f32_e32 v237, v237
	v_rcp_f32_e32 v255, v255
	v_exp_f32_e32 v234, v234
	v_exp_f32_e32 v252, v252
	v_exp_f32_e32 v235, v235
	v_exp_f32_e32 v253, v253
	v_pk_fma_f32 v[238:239], v[236:237], s[80:81], v[248:249] op_sel_hi:[1,0,1]
	v_pk_fma_f32 v[70:71], v[254:255], s[80:81], v[248:249] op_sel_hi:[1,0,1]
	v_pk_mul_f32 v[240:241], v[232:233], v[34:35] op_sel_hi:[0,1]
	v_pk_mul_f32 v[72:73], v[232:233], v[36:37] op_sel_hi:[0,1]
	v_pk_fma_f32 v[238:239], v[238:239], v[236:237], s[82:83] op_sel_hi:[1,1,0]
	v_pk_fma_f32 v[70:71], v[70:71], v[254:255], s[82:83] op_sel_hi:[1,1,0]
	v_pk_fma_f32 v[238:239], v[238:239], v[236:237], s[84:85] op_sel_hi:[1,1,0]
	v_pk_fma_f32 v[70:71], v[70:71], v[254:255], s[84:85] op_sel_hi:[1,1,0]
	v_pk_fma_f32 v[238:239], v[238:239], v[236:237], s[86:87] op_sel_hi:[1,1,0]
	v_pk_fma_f32 v[70:71], v[70:71], v[254:255], s[86:87] op_sel_hi:[1,1,0]
	v_pk_mul_f32 v[238:239], v[238:239], v[236:237]
	v_pk_mul_f32 v[70:71], v[70:71], v[254:255]
	v_pk_fma_f32 v[238:239], v[238:239], v[234:235], 1.0 op_sel_hi:[1,1,0] neg_lo:[1,0,0] neg_hi:[1,0,0]
	v_pk_fma_f32 v[70:71], v[70:71], v[252:253], 1.0 op_sel_hi:[1,1,0] neg_lo:[1,0,0] neg_hi:[1,0,0]
	v_fma_f32 v242, |v240|, v238, v240
	v_fma_f32 v0, |v72|, v70, v72
	v_fma_f32 v243, |v241|, v239, v241
	v_fma_f32 v1, |v73|, v71, v73
	v_cvt_pk_f16_f32 v246, v242, v243
	v_cvt_pk_f16_f32 v247, v0, v1
	v_cmp_lt_i32_e32 vcc, -1, v202
	s_nop 0
	v_permlane16_swap_b32_e32 v244, v246
	v_permlane16_swap_b32_e32 v245, v247
	s_and_saveexec_b64 s[10:11], vcc
	s_cbranch_execz .Lep_4
	v_mov_b32_e32 v250, v202
	v_mov_b32_e32 v251, 0
	v_lshlrev_b64 v[250:251], 10, v[250:251]
	v_lshl_add_u64 v[250:251], v[78:79], 0, v[250:251]
	global_store_dwordx4 v[250:251], v[244:247], off sc1

.Lepskip_4:
	v_cmp_lt_i32_e32 vcc, -1, v198
	s_cbranch_vccz .Lepskip_5
	v_mul_f32_e32 v232, 0.5, v200
	v_pk_mul_f32 v[234:235], v[30:31], v[30:31]
	v_pk_mul_f32 v[252:253], v[32:33], v[32:33]
	v_fma_f32 v236, |v30|, s76, 1.0
	v_fma_f32 v254, |v32|, s76, 1.0
	v_fma_f32 v237, |v31|, s76, 1.0
	v_fma_f32 v255, |v33|, s76, 1.0
	v_pk_mul_f32 v[234:235], v[234:235], s[78:79] op_sel_hi:[1,0]
	v_pk_mul_f32 v[252:253], v[252:253], s[78:79] op_sel_hi:[1,0]
	v_rcp_f32_e32 v236, v236
	v_rcp_f32_e32 v254, v254
	v_rcp_f32_e32 v237, v237
	v_rcp_f32_e32 v255, v255
	v_exp_f32_e32 v234, v234
	v_exp_f32_e32 v252, v252
	v_exp_f32_e32 v235, v235
	v_exp_f32_e32 v253, v253
	v_pk_fma_f32 v[238:239], v[236:237], s[80:81], v[248:249] op_sel_hi:[1,0,1]
	v_pk_fma_f32 v[70:71], v[254:255], s[80:81], v[248:249] op_sel_hi:[1,0,1]
	v_pk_mul_f32 v[240:241], v[232:233], v[30:31] op_sel_hi:[0,1]
	v_pk_mul_f32 v[72:73], v[232:233], v[32:33] op_sel_hi:[0,1]
	v_pk_fma_f32 v[238:239], v[238:239], v[236:237], s[82:83] op_sel_hi:[1,1,0]
	v_pk_fma_f32 v[70:71], v[70:71], v[254:255], s[82:83] op_sel_hi:[1,1,0]
	v_pk_fma_f32 v[238:239], v[238:239], v[236:237], s[84:85] op_sel_hi:[1,1,0]
	v_pk_fma_f32 v[70:71], v[70:71], v[254:255], s[84:85] op_sel_hi:[1,1,0]
	v_pk_fma_f32 v[238:239], v[238:239], v[236:237], s[86:87] op_sel_hi:[1,1,0]
	v_pk_fma_f32 v[70:71], v[70:71], v[254:255], s[86:87] op_sel_hi:[1,1,0]
	v_pk_mul_f32 v[238:239], v[238:239], v[236:237]
	v_pk_mul_f32 v[70:71], v[70:71], v[254:255]
	v_pk_fma_f32 v[238:239], v[238:239], v[234:235], 1.0 op_sel_hi:[1,1,0] neg_lo:[1,0,0] neg_hi:[1,0,0]
	v_pk_fma_f32 v[70:71], v[70:71], v[252:253], 1.0 op_sel_hi:[1,1,0] neg_lo:[1,0,0] neg_hi:[1,0,0]
	v_fma_f32 v242, |v240|, v238, v240
	v_fma_f32 v0, |v72|, v70, v72
	v_fma_f32 v243, |v241|, v239, v241
	v_fma_f32 v1, |v73|, v71, v73
	v_cvt_pk_f16_f32 v244, v242, v243
	v_cvt_pk_f16_f32 v245, v0, v1
	v_pk_mul_f32 v[234:235], v[26:27], v[26:27]
	v_pk_mul_f32 v[252:253], v[28:29], v[28:29]
	v_fma_f32 v236, |v26|, s76, 1.0
	v_fma_f32 v254, |v28|, s76, 1.0
	v_fma_f32 v237, |v27|, s76, 1.0
	v_fma_f32 v255, |v29|, s76, 1.0
	v_pk_mul_f32 v[234:235], v[234:235], s[78:79] op_sel_hi:[1,0]
	v_pk_mul_f32 v[252:253], v[252:253], s[78:79] op_sel_hi:[1,0]
	v_rcp_f32_e32 v236, v236
	v_rcp_f32_e32 v254, v254
	v_rcp_f32_e32 v237, v237
	v_rcp_f32_e32 v255, v255
	v_exp_f32_e32 v234, v234
	v_exp_f32_e32 v252, v252
	v_exp_f32_e32 v235, v235
	v_exp_f32_e32 v253, v253
	v_pk_fma_f32 v[238:239], v[236:237], s[80:81], v[248:249] op_sel_hi:[1,0,1]
	v_pk_fma_f32 v[70:71], v[254:255], s[80:81], v[248:249] op_sel_hi:[1,0,1]
	v_pk_mul_f32 v[240:241], v[232:233], v[26:27] op_sel_hi:[0,1]
	v_pk_mul_f32 v[72:73], v[232:233], v[28:29] op_sel_hi:[0,1]
	v_pk_fma_f32 v[238:239], v[238:239], v[236:237], s[82:83] op_sel_hi:[1,1,0]
	v_pk_fma_f32 v[70:71], v[70:71], v[254:255], s[82:83] op_sel_hi:[1,1,0]
	v_pk_fma_f32 v[238:239], v[238:239], v[236:237], s[84:85] op_sel_hi:[1,1,0]
	v_pk_fma_f32 v[70:71], v[70:71], v[254:255], s[84:85] op_sel_hi:[1,1,0]
	v_pk_fma_f32 v[238:239], v[238:239], v[236:237], s[86:87] op_sel_hi:[1,1,0]
	v_pk_fma_f32 v[70:71], v[70:71], v[254:255], s[86:87] op_sel_hi:[1,1,0]
	v_pk_mul_f32 v[238:239], v[238:239], v[236:237]
	v_pk_mul_f32 v[70:71], v[70:71], v[254:255]
	v_pk_fma_f32 v[238:239], v[238:239], v[234:235], 1.0 op_sel_hi:[1,1,0] neg_lo:[1,0,0] neg_hi:[1,0,0]
	v_pk_fma_f32 v[70:71], v[70:71], v[252:253], 1.0 op_sel_hi:[1,1,0] neg_lo:[1,0,0] neg_hi:[1,0,0]
	v_fma_f32 v242, |v240|, v238, v240
	v_fma_f32 v0, |v72|, v70, v72
	v_fma_f32 v243, |v241|, v239, v241
	v_fma_f32 v1, |v73|, v71, v73
	v_cvt_pk_f16_f32 v246, v242, v243
	v_cvt_pk_f16_f32 v247, v0, v1
	v_cmp_lt_i32_e32 vcc, -1, v198
	s_nop 0
	v_permlane16_swap_b32_e32 v244, v246
	v_permlane16_swap_b32_e32 v245, v247
	s_and_saveexec_b64 s[10:11], vcc
	s_cbranch_execz .Lep_5
	v_mov_b32_e32 v250, v198
	v_mov_b32_e32 v251, 0
	v_lshlrev_b64 v[250:251], 10, v[250:251]
	v_lshl_add_u64 v[250:251], v[78:79], 0, v[250:251]
	global_store_dwordx4 v[250:251], v[244:247], off sc1

.Lepskip_5:
	v_cmp_lt_i32_e32 vcc, -1, v194
	s_cbranch_vccz .Lepskip_6
	v_mul_f32_e32 v232, 0.5, v196
	v_pk_mul_f32 v[234:235], v[22:23], v[22:23]
	v_pk_mul_f32 v[252:253], v[24:25], v[24:25]
	v_fma_f32 v236, |v22|, s76, 1.0
	v_fma_f32 v254, |v24|, s76, 1.0
	v_fma_f32 v237, |v23|, s76, 1.0
	v_fma_f32 v255, |v25|, s76, 1.0
	v_pk_mul_f32 v[234:235], v[234:235], s[78:79] op_sel_hi:[1,0]
	v_pk_mul_f32 v[252:253], v[252:253], s[78:79] op_sel_hi:[1,0]
	v_rcp_f32_e32 v236, v236
	v_rcp_f32_e32 v254, v254
	v_rcp_f32_e32 v237, v237
	v_rcp_f32_e32 v255, v255
	v_exp_f32_e32 v234, v234
	v_exp_f32_e32 v252, v252
	v_exp_f32_e32 v235, v235
	v_exp_f32_e32 v253, v253
	v_pk_fma_f32 v[238:239], v[236:237], s[80:81], v[248:249] op_sel_hi:[1,0,1]
	v_pk_fma_f32 v[70:71], v[254:255], s[80:81], v[248:249] op_sel_hi:[1,0,1]
	v_pk_mul_f32 v[240:241], v[232:233], v[22:23] op_sel_hi:[0,1]
	v_pk_mul_f32 v[72:73], v[232:233], v[24:25] op_sel_hi:[0,1]
	v_pk_fma_f32 v[238:239], v[238:239], v[236:237], s[82:83] op_sel_hi:[1,1,0]
	v_pk_fma_f32 v[70:71], v[70:71], v[254:255], s[82:83] op_sel_hi:[1,1,0]
	v_pk_fma_f32 v[238:239], v[238:239], v[236:237], s[84:85] op_sel_hi:[1,1,0]
	v_pk_fma_f32 v[70:71], v[70:71], v[254:255], s[84:85] op_sel_hi:[1,1,0]
	v_pk_fma_f32 v[238:239], v[238:239], v[236:237], s[86:87] op_sel_hi:[1,1,0]
	v_pk_fma_f32 v[70:71], v[70:71], v[254:255], s[86:87] op_sel_hi:[1,1,0]
	v_pk_mul_f32 v[238:239], v[238:239], v[236:237]
	v_pk_mul_f32 v[70:71], v[70:71], v[254:255]
	v_pk_fma_f32 v[238:239], v[238:239], v[234:235], 1.0 op_sel_hi:[1,1,0] neg_lo:[1,0,0] neg_hi:[1,0,0]
	v_pk_fma_f32 v[70:71], v[70:71], v[252:253], 1.0 op_sel_hi:[1,1,0] neg_lo:[1,0,0] neg_hi:[1,0,0]
	v_fma_f32 v242, |v240|, v238, v240
	v_fma_f32 v0, |v72|, v70, v72
	v_fma_f32 v243, |v241|, v239, v241
	v_fma_f32 v1, |v73|, v71, v73
	v_cvt_pk_f16_f32 v244, v242, v243
	v_cvt_pk_f16_f32 v245, v0, v1
	v_pk_mul_f32 v[234:235], v[18:19], v[18:19]
	v_pk_mul_f32 v[252:253], v[20:21], v[20:21]
	v_fma_f32 v236, |v18|, s76, 1.0
	v_fma_f32 v254, |v20|, s76, 1.0
	v_fma_f32 v237, |v19|, s76, 1.0
	v_fma_f32 v255, |v21|, s76, 1.0
	v_pk_mul_f32 v[234:235], v[234:235], s[78:79] op_sel_hi:[1,0]
	v_pk_mul_f32 v[252:253], v[252:253], s[78:79] op_sel_hi:[1,0]
	v_rcp_f32_e32 v236, v236
	v_rcp_f32_e32 v254, v254
	v_rcp_f32_e32 v237, v237
	v_rcp_f32_e32 v255, v255
	v_exp_f32_e32 v234, v234
	v_exp_f32_e32 v252, v252
	v_exp_f32_e32 v235, v235
	v_exp_f32_e32 v253, v253
	v_pk_fma_f32 v[238:239], v[236:237], s[80:81], v[248:249] op_sel_hi:[1,0,1]
	v_pk_fma_f32 v[70:71], v[254:255], s[80:81], v[248:249] op_sel_hi:[1,0,1]
	v_pk_mul_f32 v[240:241], v[232:233], v[18:19] op_sel_hi:[0,1]
	v_pk_mul_f32 v[72:73], v[232:233], v[20:21] op_sel_hi:[0,1]
	v_pk_fma_f32 v[238:239], v[238:239], v[236:237], s[82:83] op_sel_hi:[1,1,0]
	v_pk_fma_f32 v[70:71], v[70:71], v[254:255], s[82:83] op_sel_hi:[1,1,0]
	v_pk_fma_f32 v[238:239], v[238:239], v[236:237], s[84:85] op_sel_hi:[1,1,0]
	v_pk_fma_f32 v[70:71], v[70:71], v[254:255], s[84:85] op_sel_hi:[1,1,0]
	v_pk_fma_f32 v[238:239], v[238:239], v[236:237], s[86:87] op_sel_hi:[1,1,0]
	v_pk_fma_f32 v[70:71], v[70:71], v[254:255], s[86:87] op_sel_hi:[1,1,0]
	v_pk_mul_f32 v[238:239], v[238:239], v[236:237]
	v_pk_mul_f32 v[70:71], v[70:71], v[254:255]
	v_pk_fma_f32 v[238:239], v[238:239], v[234:235], 1.0 op_sel_hi:[1,1,0] neg_lo:[1,0,0] neg_hi:[1,0,0]
	v_pk_fma_f32 v[70:71], v[70:71], v[252:253], 1.0 op_sel_hi:[1,1,0] neg_lo:[1,0,0] neg_hi:[1,0,0]
	v_fma_f32 v242, |v240|, v238, v240
	v_fma_f32 v0, |v72|, v70, v72
	v_fma_f32 v243, |v241|, v239, v241
	v_fma_f32 v1, |v73|, v71, v73
	v_cvt_pk_f16_f32 v246, v242, v243
	v_cvt_pk_f16_f32 v247, v0, v1
	v_cmp_lt_i32_e32 vcc, -1, v194
	s_nop 0
	v_permlane16_swap_b32_e32 v244, v246
	v_permlane16_swap_b32_e32 v245, v247
	s_and_saveexec_b64 s[10:11], vcc
	s_cbranch_execz .Lep_6
	v_mov_b32_e32 v250, v194
	v_mov_b32_e32 v251, 0
	v_lshlrev_b64 v[250:251], 10, v[250:251]
	v_lshl_add_u64 v[250:251], v[78:79], 0, v[250:251]
	global_store_dwordx4 v[250:251], v[244:247], off sc1

.Lepskip_6:
	v_cmp_lt_i32_e32 vcc, -1, v190
	s_cbranch_vccz .Lepskip_7
	v_mul_f32_e32 v232, 0.5, v192
	v_pk_mul_f32 v[234:235], v[14:15], v[14:15]
	v_pk_mul_f32 v[252:253], v[16:17], v[16:17]
	v_fma_f32 v236, |v14|, s76, 1.0
	v_fma_f32 v254, |v16|, s76, 1.0
	v_fma_f32 v237, |v15|, s76, 1.0
	v_fma_f32 v255, |v17|, s76, 1.0
	v_pk_mul_f32 v[234:235], v[234:235], s[78:79] op_sel_hi:[1,0]
	v_pk_mul_f32 v[252:253], v[252:253], s[78:79] op_sel_hi:[1,0]
	v_rcp_f32_e32 v236, v236
	v_rcp_f32_e32 v254, v254
	v_rcp_f32_e32 v237, v237
	v_rcp_f32_e32 v255, v255
	v_exp_f32_e32 v234, v234
	v_exp_f32_e32 v252, v252
	v_exp_f32_e32 v235, v235
	v_exp_f32_e32 v253, v253
	v_pk_fma_f32 v[238:239], v[236:237], s[80:81], v[248:249] op_sel_hi:[1,0,1]
	v_pk_fma_f32 v[70:71], v[254:255], s[80:81], v[248:249] op_sel_hi:[1,0,1]
	v_pk_mul_f32 v[240:241], v[232:233], v[14:15] op_sel_hi:[0,1]
	v_pk_mul_f32 v[72:73], v[232:233], v[16:17] op_sel_hi:[0,1]
	v_pk_fma_f32 v[238:239], v[238:239], v[236:237], s[82:83] op_sel_hi:[1,1,0]
	v_pk_fma_f32 v[70:71], v[70:71], v[254:255], s[82:83] op_sel_hi:[1,1,0]
	v_pk_fma_f32 v[238:239], v[238:239], v[236:237], s[84:85] op_sel_hi:[1,1,0]
	v_pk_fma_f32 v[70:71], v[70:71], v[254:255], s[84:85] op_sel_hi:[1,1,0]
	v_pk_fma_f32 v[238:239], v[238:239], v[236:237], s[86:87] op_sel_hi:[1,1,0]
	v_pk_fma_f32 v[70:71], v[70:71], v[254:255], s[86:87] op_sel_hi:[1,1,0]
	v_pk_mul_f32 v[238:239], v[238:239], v[236:237]
	v_pk_mul_f32 v[70:71], v[70:71], v[254:255]
	v_pk_fma_f32 v[238:239], v[238:239], v[234:235], 1.0 op_sel_hi:[1,1,0] neg_lo:[1,0,0] neg_hi:[1,0,0]
	v_pk_fma_f32 v[70:71], v[70:71], v[252:253], 1.0 op_sel_hi:[1,1,0] neg_lo:[1,0,0] neg_hi:[1,0,0]
	v_fma_f32 v242, |v240|, v238, v240
	v_fma_f32 v0, |v72|, v70, v72
	v_fma_f32 v243, |v241|, v239, v241
	v_fma_f32 v1, |v73|, v71, v73
	v_cvt_pk_f16_f32 v244, v242, v243
	v_cvt_pk_f16_f32 v245, v0, v1
	v_pk_mul_f32 v[234:235], v[10:11], v[10:11]
	v_pk_mul_f32 v[252:253], v[12:13], v[12:13]
	v_fma_f32 v236, |v10|, s76, 1.0
	v_fma_f32 v254, |v12|, s76, 1.0
	v_fma_f32 v237, |v11|, s76, 1.0
	v_fma_f32 v255, |v13|, s76, 1.0
	v_pk_mul_f32 v[234:235], v[234:235], s[78:79] op_sel_hi:[1,0]
	v_pk_mul_f32 v[252:253], v[252:253], s[78:79] op_sel_hi:[1,0]
	v_rcp_f32_e32 v236, v236
	v_rcp_f32_e32 v254, v254
	v_rcp_f32_e32 v237, v237
	v_rcp_f32_e32 v255, v255
	v_exp_f32_e32 v234, v234
	v_exp_f32_e32 v252, v252
	v_exp_f32_e32 v235, v235
	v_exp_f32_e32 v253, v253
	v_pk_fma_f32 v[238:239], v[236:237], s[80:81], v[248:249] op_sel_hi:[1,0,1]
	v_pk_fma_f32 v[70:71], v[254:255], s[80:81], v[248:249] op_sel_hi:[1,0,1]
	v_pk_mul_f32 v[240:241], v[232:233], v[10:11] op_sel_hi:[0,1]
	v_pk_mul_f32 v[72:73], v[232:233], v[12:13] op_sel_hi:[0,1]
	v_pk_fma_f32 v[238:239], v[238:239], v[236:237], s[82:83] op_sel_hi:[1,1,0]
	v_pk_fma_f32 v[70:71], v[70:71], v[254:255], s[82:83] op_sel_hi:[1,1,0]
	v_pk_fma_f32 v[238:239], v[238:239], v[236:237], s[84:85] op_sel_hi:[1,1,0]
	v_pk_fma_f32 v[70:71], v[70:71], v[254:255], s[84:85] op_sel_hi:[1,1,0]
	v_pk_fma_f32 v[238:239], v[238:239], v[236:237], s[86:87] op_sel_hi:[1,1,0]
	v_pk_fma_f32 v[70:71], v[70:71], v[254:255], s[86:87] op_sel_hi:[1,1,0]
	v_pk_mul_f32 v[238:239], v[238:239], v[236:237]
	v_pk_mul_f32 v[70:71], v[70:71], v[254:255]
	v_pk_fma_f32 v[238:239], v[238:239], v[234:235], 1.0 op_sel_hi:[1,1,0] neg_lo:[1,0,0] neg_hi:[1,0,0]
	v_pk_fma_f32 v[70:71], v[70:71], v[252:253], 1.0 op_sel_hi:[1,1,0] neg_lo:[1,0,0] neg_hi:[1,0,0]
	v_fma_f32 v242, |v240|, v238, v240
	v_fma_f32 v0, |v72|, v70, v72
	v_fma_f32 v243, |v241|, v239, v241
	v_fma_f32 v1, |v73|, v71, v73
	v_cvt_pk_f16_f32 v246, v242, v243
	v_cvt_pk_f16_f32 v247, v0, v1
	v_cmp_lt_i32_e32 vcc, -1, v190
	s_nop 0
	v_permlane16_swap_b32_e32 v244, v246
	v_permlane16_swap_b32_e32 v245, v247
	s_and_saveexec_b64 s[10:11], vcc
	s_cbranch_execz .Lep_7
	v_mov_b32_e32 v250, v190
	v_mov_b32_e32 v251, 0
	v_lshlrev_b64 v[250:251], 10, v[250:251]
	v_lshl_add_u64 v[250:251], v[78:79], 0, v[250:251]
	global_store_dwordx4 v[250:251], v[244:247], off sc1

.Lepskip_7:
	v_cmp_lt_i32_e32 vcc, -1, v186
	s_cbranch_vccz .Lepskip_8
	v_mul_f32_e32 v232, 0.5, v188
	v_pk_mul_f32 v[234:235], v[6:7], v[6:7]
	v_pk_mul_f32 v[252:253], v[8:9], v[8:9]
	v_fma_f32 v236, |v6|, s76, 1.0
	v_fma_f32 v254, |v8|, s76, 1.0
	v_fma_f32 v237, |v7|, s76, 1.0
	v_fma_f32 v255, |v9|, s76, 1.0
	v_pk_mul_f32 v[234:235], v[234:235], s[78:79] op_sel_hi:[1,0]
	v_pk_mul_f32 v[252:253], v[252:253], s[78:79] op_sel_hi:[1,0]
	v_rcp_f32_e32 v236, v236
	v_rcp_f32_e32 v254, v254
	v_rcp_f32_e32 v237, v237
	v_rcp_f32_e32 v255, v255
	v_exp_f32_e32 v234, v234
	v_exp_f32_e32 v252, v252
	v_exp_f32_e32 v235, v235
	v_exp_f32_e32 v253, v253
	v_pk_fma_f32 v[238:239], v[236:237], s[80:81], v[248:249] op_sel_hi:[1,0,1]
	v_pk_fma_f32 v[70:71], v[254:255], s[80:81], v[248:249] op_sel_hi:[1,0,1]
	v_pk_mul_f32 v[240:241], v[232:233], v[6:7] op_sel_hi:[0,1]
	v_pk_mul_f32 v[72:73], v[232:233], v[8:9] op_sel_hi:[0,1]
	v_pk_fma_f32 v[238:239], v[238:239], v[236:237], s[82:83] op_sel_hi:[1,1,0]
	v_pk_fma_f32 v[70:71], v[70:71], v[254:255], s[82:83] op_sel_hi:[1,1,0]
	v_pk_fma_f32 v[238:239], v[238:239], v[236:237], s[84:85] op_sel_hi:[1,1,0]
	v_pk_fma_f32 v[70:71], v[70:71], v[254:255], s[84:85] op_sel_hi:[1,1,0]
	v_pk_fma_f32 v[238:239], v[238:239], v[236:237], s[86:87] op_sel_hi:[1,1,0]
	v_pk_fma_f32 v[70:71], v[70:71], v[254:255], s[86:87] op_sel_hi:[1,1,0]
	v_pk_mul_f32 v[238:239], v[238:239], v[236:237]
	v_pk_mul_f32 v[70:71], v[70:71], v[254:255]
	v_pk_fma_f32 v[238:239], v[238:239], v[234:235], 1.0 op_sel_hi:[1,1,0] neg_lo:[1,0,0] neg_hi:[1,0,0]
	v_pk_fma_f32 v[70:71], v[70:71], v[252:253], 1.0 op_sel_hi:[1,1,0] neg_lo:[1,0,0] neg_hi:[1,0,0]
	v_fma_f32 v242, |v240|, v238, v240
	v_fma_f32 v0, |v72|, v70, v72
	v_fma_f32 v243, |v241|, v239, v241
	v_fma_f32 v1, |v73|, v71, v73
	v_cvt_pk_f16_f32 v244, v242, v243
	v_cvt_pk_f16_f32 v245, v0, v1
	v_pk_mul_f32 v[234:235], v[2:3], v[2:3]
	v_pk_mul_f32 v[252:253], v[4:5], v[4:5]
	v_fma_f32 v236, |v2|, s76, 1.0
	v_fma_f32 v254, |v4|, s76, 1.0
	v_fma_f32 v237, |v3|, s76, 1.0
	v_fma_f32 v255, |v5|, s76, 1.0
	v_pk_mul_f32 v[234:235], v[234:235], s[78:79] op_sel_hi:[1,0]
	v_pk_mul_f32 v[252:253], v[252:253], s[78:79] op_sel_hi:[1,0]
	v_rcp_f32_e32 v236, v236
	v_rcp_f32_e32 v254, v254
	v_rcp_f32_e32 v237, v237
	v_rcp_f32_e32 v255, v255
	v_exp_f32_e32 v234, v234
	v_exp_f32_e32 v252, v252
	v_exp_f32_e32 v235, v235
	v_exp_f32_e32 v253, v253
	v_pk_fma_f32 v[238:239], v[236:237], s[80:81], v[248:249] op_sel_hi:[1,0,1]
	v_pk_fma_f32 v[70:71], v[254:255], s[80:81], v[248:249] op_sel_hi:[1,0,1]
	v_pk_mul_f32 v[240:241], v[232:233], v[2:3] op_sel_hi:[0,1]
	v_pk_mul_f32 v[72:73], v[232:233], v[4:5] op_sel_hi:[0,1]
	v_pk_fma_f32 v[238:239], v[238:239], v[236:237], s[82:83] op_sel_hi:[1,1,0]
	v_pk_fma_f32 v[70:71], v[70:71], v[254:255], s[82:83] op_sel_hi:[1,1,0]
	v_pk_fma_f32 v[238:239], v[238:239], v[236:237], s[84:85] op_sel_hi:[1,1,0]
	v_pk_fma_f32 v[70:71], v[70:71], v[254:255], s[84:85] op_sel_hi:[1,1,0]
	v_pk_fma_f32 v[238:239], v[238:239], v[236:237], s[86:87] op_sel_hi:[1,1,0]
	v_pk_fma_f32 v[70:71], v[70:71], v[254:255], s[86:87] op_sel_hi:[1,1,0]
	v_pk_mul_f32 v[238:239], v[238:239], v[236:237]
	v_pk_mul_f32 v[70:71], v[70:71], v[254:255]
	v_pk_fma_f32 v[238:239], v[238:239], v[234:235], 1.0 op_sel_hi:[1,1,0] neg_lo:[1,0,0] neg_hi:[1,0,0]
	v_pk_fma_f32 v[70:71], v[70:71], v[252:253], 1.0 op_sel_hi:[1,1,0] neg_lo:[1,0,0] neg_hi:[1,0,0]
	v_fma_f32 v242, |v240|, v238, v240
	v_fma_f32 v0, |v72|, v70, v72
	v_fma_f32 v243, |v241|, v239, v241
	v_fma_f32 v1, |v73|, v71, v73
	v_cvt_pk_f16_f32 v246, v242, v243
	v_cvt_pk_f16_f32 v247, v0, v1
	v_cmp_lt_i32_e32 vcc, -1, v186
	s_nop 0
	v_permlane16_swap_b32_e32 v244, v246
	v_permlane16_swap_b32_e32 v245, v247
	s_and_saveexec_b64 s[10:11], vcc
	s_cbranch_execz .Lep_8
	v_mov_b32_e32 v250, v186
	v_mov_b32_e32 v251, 0
	v_lshlrev_b64 v[250:251], 10, v[250:251]
	v_lshl_add_u64 v[250:251], v[78:79], 0, v[250:251]
	global_store_dwordx4 v[250:251], v[244:247], off sc1

.Lepskip_8:
.LBB2_132:
	s_endpgm
	.p2align	8
